# grid barrier: L1 invalidate issued right after the arrival atomic (only sc1 polls follow until release), post-release invalidates removed
# speedup vs baseline: 1.0055x; 1.0055x over previous
.LBB0_193:
	s_lshl_b32 s4, s46, 8
	s_add_u32 s4, s2, s4
	s_addc_u32 s5, s3, 0
	v_mov_b32_e32 v1, 0x5000
	v_mov_b32_e32 v3, 1
	global_atomic_add v3, v1, v3, s[4:5] offset:1024 sc0
	buffer_inv sc1
	v_cvt_f32_u32_e32 v1, v2
	v_sub_u32_e32 v4, 0, v2
	s_add_u32 s4, s4, 0x4000
	s_addc_u32 s5, s5, 0
	v_rcp_iflag_f32_e32 v1, v1
	s_nop 0
	v_mul_f32_e32 v1, 0x4f7ffffe, v1
	v_cvt_u32_f32_e32 v1, v1
	v_mul_lo_u32 v4, v4, v1
	v_mul_hi_u32 v4, v1, v4
	v_add_u32_e32 v1, v1, v4
	s_waitcnt vmcnt(1)
	v_mul_hi_u32 v1, v3, v1
	v_mul_lo_u32 v4, v1, v2
	v_sub_u32_e32 v4, v3, v4
	v_add_u32_e32 v5, 1, v1
	v_cmp_ge_u32_e32 vcc, v4, v2
	v_add_u32_e32 v3, 1, v3
	s_nop 0
	v_cndmask_b32_e32 v1, v1, v5, vcc
	v_sub_u32_e32 v5, v4, v2
	v_cndmask_b32_e32 v4, v4, v5, vcc
	v_add_u32_e32 v5, 1, v1
	v_cmp_ge_u32_e32 vcc, v4, v2
	s_nop 1
	v_cndmask_b32_e32 v1, v1, v5, vcc
	v_mul_lo_u32 v4, v2, v1
	v_add_u32_e32 v2, v4, v2
	v_cmp_ne_u32_e32 vcc, v3, v2
	s_and_saveexec_b64 s[6:7], vcc
	s_xor_b64 s[6:7], exec, s[6:7]
	s_cbranch_execz .LBB0_207
	s_waitcnt lgkmcnt(0)
	v_mov_b32_e32 v0, 0x2000
	global_load_dword v0, v0, s[4:5] offset:1024 sc1
	s_add_u32 s12, s4, 0x2400
	s_addc_u32 s13, s5, 0
	s_waitcnt vmcnt(0)
	v_cmp_eq_u32_e32 vcc, v0, v1
	s_and_saveexec_b64 s[8:9], vcc
	s_cbranch_execz .LBB0_206
	s_add_u32 s10, s2, 0x4200
	s_addc_u32 s11, s3, 0
	s_mov_b32 s24, 1
	s_mov_b64 s[14:15], 0
	v_mov_b32_e32 v0, 0
	s_branch .LBB0_197

.LBB0_206:
	s_or_b64 exec, exec, s[8:9]
	s_waitcnt vmcnt(0)
	s_waitcnt vmcnt(0)

.LBB0_224:
	s_or_b64 exec, exec, s[2:3]
	v_mov_b32_e32 v0, 0x2000
	v_mov_b32_e32 v1, 1
	s_waitcnt vmcnt(0)
	global_atomic_add v0, v1, s[4:5] offset:1024
	s_waitcnt vmcnt(0)

.LBB0_227:
	s_or_b64 exec, exec, s[4:5]
	v_mov_b32_e32 v0, 0x2000
	s_waitcnt vmcnt(0)
	global_atomic_add v0, v239, s[6:7] offset:1024
	s_waitcnt vmcnt(0)

.LBB0_300:
	v_readlane_b32 s6, v252, 52
	s_lshl_b32 s6, s6, 2
	s_add_u32 s6, s4, s6
	s_addc_u32 s7, s5, 0
	v_mov_b32_e32 v1, 0x5000
	v_sub_u32_e32 v4, 0, v2
	global_atomic_add v3, v1, v239, s[6:7] offset:1024 sc0
	buffer_inv sc1
	v_cvt_f32_u32_e32 v1, v2
	s_add_u32 s6, s6, 0x4000
	s_addc_u32 s7, s7, 0
	v_rcp_iflag_f32_e32 v1, v1
	s_nop 0
	v_mul_f32_e32 v1, 0x4f7ffffe, v1
	v_cvt_u32_f32_e32 v1, v1
	v_mul_lo_u32 v4, v4, v1
	v_mul_hi_u32 v4, v1, v4
	v_add_u32_e32 v1, v1, v4
	s_waitcnt vmcnt(1)
	v_mul_hi_u32 v1, v3, v1
	v_mul_lo_u32 v4, v1, v2
	v_sub_u32_e32 v4, v3, v4
	v_add_u32_e32 v5, 1, v1
	v_cmp_ge_u32_e32 vcc, v4, v2
	v_add_u32_e32 v3, 1, v3
	s_nop 0
	v_cndmask_b32_e32 v1, v1, v5, vcc
	v_sub_u32_e32 v5, v4, v2
	v_cndmask_b32_e32 v4, v4, v5, vcc
	v_add_u32_e32 v5, 1, v1
	v_cmp_ge_u32_e32 vcc, v4, v2
	s_nop 1
	v_cndmask_b32_e32 v1, v1, v5, vcc
	v_mul_lo_u32 v4, v2, v1
	v_add_u32_e32 v2, v4, v2
	v_cmp_ne_u32_e32 vcc, v3, v2
	s_and_saveexec_b64 s[8:9], vcc
	s_xor_b64 s[8:9], exec, s[8:9]
	s_cbranch_execz .LBB0_314
	s_waitcnt lgkmcnt(0)
	v_mov_b32_e32 v0, 0x2000
	global_load_dword v0, v0, s[6:7] offset:1024 sc1
	s_add_u32 s14, s6, 0x2400
	s_addc_u32 s15, s7, 0
	s_waitcnt vmcnt(0)
	v_cmp_eq_u32_e32 vcc, v0, v1
	s_and_saveexec_b64 s[10:11], vcc
	s_cbranch_execz .LBB0_313
	s_add_u32 s12, s4, 0x4200
	s_addc_u32 s13, s5, 0
	s_mov_b32 s26, 1
	s_mov_b64 s[16:17], 0
	s_branch .LBB0_304

.LBB0_313:
	s_or_b64 exec, exec, s[10:11]
	s_waitcnt vmcnt(0)
	s_waitcnt vmcnt(0)

.LBB0_383:
	v_readlane_b32 s8, v252, 52
	s_lshl_b32 s8, s8, 2
	s_add_u32 s8, s6, s8
	s_addc_u32 s9, s7, 0
	v_mov_b32_e32 v1, 0x5000
	v_sub_u32_e32 v4, 0, v2
	global_atomic_add v3, v1, v239, s[8:9] offset:1024 sc0
	buffer_inv sc1
	v_cvt_f32_u32_e32 v1, v2
	s_add_u32 s8, s8, 0x4000
	s_addc_u32 s9, s9, 0
	v_rcp_iflag_f32_e32 v1, v1
	s_nop 0
	v_mul_f32_e32 v1, 0x4f7ffffe, v1
	v_cvt_u32_f32_e32 v1, v1
	v_mul_lo_u32 v4, v4, v1
	v_mul_hi_u32 v4, v1, v4
	v_add_u32_e32 v1, v1, v4
	s_waitcnt vmcnt(1)
	v_mul_hi_u32 v1, v3, v1
	v_mul_lo_u32 v4, v1, v2
	v_sub_u32_e32 v4, v3, v4
	v_add_u32_e32 v5, 1, v1
	v_cmp_ge_u32_e32 vcc, v4, v2
	v_add_u32_e32 v3, 1, v3
	s_nop 0
	v_cndmask_b32_e32 v1, v1, v5, vcc
	v_sub_u32_e32 v5, v4, v2
	v_cndmask_b32_e32 v4, v4, v5, vcc
	v_add_u32_e32 v5, 1, v1
	v_cmp_ge_u32_e32 vcc, v4, v2
	s_nop 1
	v_cndmask_b32_e32 v1, v1, v5, vcc
	v_mul_lo_u32 v4, v2, v1
	v_add_u32_e32 v2, v4, v2
	v_cmp_ne_u32_e32 vcc, v3, v2
	s_and_saveexec_b64 s[10:11], vcc
	s_xor_b64 s[10:11], exec, s[10:11]
	s_cbranch_execz .LBB0_397
	s_waitcnt lgkmcnt(0)
	v_mov_b32_e32 v0, 0x2000
	global_load_dword v0, v0, s[8:9] offset:1024 sc1
	s_add_u32 s16, s8, 0x2400
	s_addc_u32 s17, s9, 0
	s_waitcnt vmcnt(0)
	v_cmp_eq_u32_e32 vcc, v0, v1
	s_and_saveexec_b64 s[12:13], vcc
	s_cbranch_execz .LBB0_396
	s_add_u32 s14, s6, 0x4200
	s_addc_u32 s15, s7, 0
	s_mov_b32 s28, 1
	s_mov_b64 s[18:19], 0
	s_branch .LBB0_387

.LBB0_396:
	s_or_b64 exec, exec, s[12:13]
	s_waitcnt vmcnt(0)
	s_waitcnt vmcnt(0)

.LBB0_414:
	s_or_b64 exec, exec, s[6:7]
	v_mov_b32_e32 v0, 0x2000
	s_waitcnt vmcnt(0)
	global_atomic_add v0, v239, s[8:9] offset:1024
	s_waitcnt vmcnt(0)
